# v33: v30 + ffn_norm_route loop edges: bottom drain vmcnt(16) (prefetch only), first-iteration wait ladder and register copies skipped from the second iteration on
# speedup vs baseline: 1.0020x; 1.0020x over previous
.LBB0_1736:
	s_or_b64 exec, exec, s[28:29]
	s_waitcnt vmcnt(16)
	s_add_i32 s34, s34, 2
	s_add_i32 s18, s18, s38
	s_cmp_eq_u32 s39, s56
	v_mov_b32_e32 v134, v217
	v_mov_b32_e32 v135, v216
	v_mov_b32_e32 v148, v215
	v_mov_b32_e32 v149, v214
	v_mov_b32_e32 v150, v213
	v_mov_b32_e32 v146, v212
	v_mov_b32_e32 v173, v218
	v_mov_b32_e32 v171, v219
	v_mov_b32_e32 v170, v220
	v_mov_b32_e32 v172, v221
	v_mov_b32_e32 v169, v222
	v_mov_b32_e32 v168, v223
	v_mov_b32_e32 v166, v224
	v_mov_b32_e32 v160, v225
	v_mov_b32_e32 v155, v226
	v_mov_b32_e32 v154, v227
	v_mov_b64_e32 v[130:131], v[96:97]
	v_mov_b64_e32 v[94:95], v[98:99]
	v_mov_b64_e32 v[84:85], v[100:101]
	v_mov_b64_e32 v[92:93], v[102:103]
	v_mov_b64_e32 v[80:81], v[104:105]
	v_mov_b64_e32 v[82:83], v[106:107]
	v_mov_b64_e32 v[86:87], v[108:109]
	v_mov_b64_e32 v[144:145], v[110:111]
	v_mov_b64_e32 v[142:143], v[112:113]
	v_mov_b64_e32 v[140:141], v[114:115]
	v_mov_b64_e32 v[128:129], v[116:117]
	v_mov_b64_e32 v[138:139], v[118:119]
	v_mov_b64_e32 v[88:89], v[120:121]
	v_mov_b64_e32 v[90:91], v[122:123]
	v_mov_b64_e32 v[132:133], v[124:125]
	v_mov_b64_e32 v[136:137], v[126:127]
	s_cbranch_scc1 .LBB0_1858

.LBB0_1739:
	s_cmp_lg_u32 s56, 1
	s_cbranch_scc1 .Ltopskip_0
	s_andn2_b64 vcc, exec, s[6:7]
	s_waitcnt vmcnt(9)
	v_mov_b32_e32 v217, v134
	s_waitcnt vmcnt(8)
	v_mov_b32_e32 v216, v135
	s_waitcnt vmcnt(7)
	v_mov_b32_e32 v215, v148
	s_waitcnt vmcnt(6)
	v_mov_b32_e32 v214, v149
	s_waitcnt vmcnt(5)
	v_mov_b32_e32 v213, v150
	s_waitcnt vmcnt(4)
	v_mov_b32_e32 v212, v146
	v_mov_b32_e32 v218, v173
	v_mov_b32_e32 v219, v171
	v_mov_b32_e32 v220, v170
	v_mov_b32_e32 v221, v172
	v_mov_b32_e32 v222, v169
	v_mov_b32_e32 v223, v168
	v_mov_b32_e32 v224, v166
	v_mov_b32_e32 v225, v160
	v_mov_b32_e32 v226, v155
	v_mov_b32_e32 v227, v154
	s_waitcnt vmcnt(0)
	v_mov_b64_e32 v[96:97], v[130:131]
	v_mov_b64_e32 v[98:99], v[94:95]
	v_mov_b64_e32 v[100:101], v[84:85]
	v_mov_b64_e32 v[102:103], v[92:93]
	v_mov_b64_e32 v[104:105], v[80:81]
	v_mov_b64_e32 v[106:107], v[82:83]
	v_mov_b64_e32 v[108:109], v[86:87]
	v_mov_b64_e32 v[110:111], v[144:145]
	v_mov_b64_e32 v[112:113], v[142:143]
	v_mov_b64_e32 v[114:115], v[140:141]
	v_mov_b64_e32 v[116:117], v[128:129]
	v_mov_b64_e32 v[118:119], v[138:139]
	v_mov_b64_e32 v[120:121], v[88:89]
	v_mov_b64_e32 v[122:123], v[90:91]
	v_mov_b64_e32 v[124:125], v[132:133]
	v_mov_b64_e32 v[126:127], v[136:137]
.Ltopskip_0:
	v_ashrrev_i32_e32 v77, 31, v76
	v_ashrrev_i32_e32 v75, 31, v74
	v_ashrrev_i32_e32 v73, 31, v72
	v_ashrrev_i32_e32 v71, 31, v70
	v_ashrrev_i32_e32 v69, 31, v68
	v_ashrrev_i32_e32 v67, 31, v66
	v_ashrrev_i32_e32 v65, 31, v64

.LBB0_5165:
	s_or_b64 exec, exec, s[28:29]
	s_waitcnt vmcnt(16)
	s_add_i32 s34, s34, 2
	s_add_i32 s18, s18, s38
	s_cmp_eq_u32 s39, s56
	v_mov_b32_e32 v134, v217
	v_mov_b32_e32 v135, v216
	v_mov_b32_e32 v148, v215
	v_mov_b32_e32 v149, v214
	v_mov_b32_e32 v150, v213
	v_mov_b32_e32 v146, v212
	v_mov_b32_e32 v173, v218
	v_mov_b32_e32 v171, v219
	v_mov_b32_e32 v170, v220
	v_mov_b32_e32 v172, v221
	v_mov_b32_e32 v169, v222
	v_mov_b32_e32 v168, v223
	v_mov_b32_e32 v166, v224
	v_mov_b32_e32 v160, v225
	v_mov_b32_e32 v155, v226
	v_mov_b32_e32 v154, v227
	v_mov_b64_e32 v[130:131], v[96:97]
	v_mov_b64_e32 v[94:95], v[98:99]
	v_mov_b64_e32 v[84:85], v[100:101]
	v_mov_b64_e32 v[92:93], v[102:103]
	v_mov_b64_e32 v[80:81], v[104:105]
	v_mov_b64_e32 v[82:83], v[106:107]
	v_mov_b64_e32 v[86:87], v[108:109]
	v_mov_b64_e32 v[144:145], v[110:111]
	v_mov_b64_e32 v[140:141], v[112:113]
	v_mov_b64_e32 v[138:139], v[114:115]
	v_mov_b64_e32 v[128:129], v[116:117]
	v_mov_b64_e32 v[136:137], v[118:119]
	v_mov_b64_e32 v[88:89], v[120:121]
	v_mov_b64_e32 v[90:91], v[122:123]
	v_mov_b64_e32 v[132:133], v[124:125]
	v_mov_b64_e32 v[142:143], v[126:127]
	s_cbranch_scc1 .LBB0_5287

.LBB0_5168:
	s_cmp_lg_u32 s56, 1
	s_cbranch_scc1 .Ltopskip_1
	s_andn2_b64 vcc, exec, s[6:7]
	s_waitcnt vmcnt(9)
	v_mov_b32_e32 v217, v134
	s_waitcnt vmcnt(8)
	v_mov_b32_e32 v216, v135
	s_waitcnt vmcnt(7)
	v_mov_b32_e32 v215, v148
	s_waitcnt vmcnt(6)
	v_mov_b32_e32 v214, v149
	s_waitcnt vmcnt(5)
	v_mov_b32_e32 v213, v150
	s_waitcnt vmcnt(4)
	v_mov_b32_e32 v212, v146
	v_mov_b32_e32 v218, v173
	v_mov_b32_e32 v219, v171
	v_mov_b32_e32 v220, v170
	v_mov_b32_e32 v221, v172
	v_mov_b32_e32 v222, v169
	v_mov_b32_e32 v223, v168
	v_mov_b32_e32 v224, v166
	v_mov_b32_e32 v225, v160
	v_mov_b32_e32 v226, v155
	v_mov_b32_e32 v227, v154
	s_waitcnt vmcnt(0)
	v_mov_b64_e32 v[96:97], v[130:131]
	v_mov_b64_e32 v[98:99], v[94:95]
	v_mov_b64_e32 v[100:101], v[84:85]
	v_mov_b64_e32 v[102:103], v[92:93]
	v_mov_b64_e32 v[104:105], v[80:81]
	v_mov_b64_e32 v[106:107], v[82:83]
	v_mov_b64_e32 v[108:109], v[86:87]
	v_mov_b64_e32 v[110:111], v[144:145]
	v_mov_b64_e32 v[112:113], v[140:141]
	v_mov_b64_e32 v[114:115], v[138:139]
	v_mov_b64_e32 v[116:117], v[128:129]
	v_mov_b64_e32 v[118:119], v[136:137]
	v_mov_b64_e32 v[120:121], v[88:89]
	v_mov_b64_e32 v[122:123], v[90:91]
	v_mov_b64_e32 v[124:125], v[132:133]
	v_mov_b64_e32 v[126:127], v[142:143]
